# early acquire-side buffer_inv extended to the two looped MoE barrier copies (all 33 sites)
# baseline (speedup 1.0000x reference)
; __device__ __forceinline__ unsigned xb_ld(unsigned* p)              { return __hip_atomic_load(p, __ATOMIC_RELAXED, __HIP_MEMORY_SCOPE_AGENT); }
; __device__ __forceinline__ unsigned xb_add(unsigned* p, unsigned v) { return __hip_atomic_fetch_add(p, v, __ATOMIC_RELAXED, __HIP_MEMORY_SCOPE_AGENT); }
; #define XB_SPIN(cond, bar) do { unsigned _sp = 0; while (cond) { __builtin_amdgcn_s_sleep(1); \
;     if ((++_sp & 255u) == 0u) { if (xb_ld(&(bar)[XB_TMO])) break; if (_sp > XB_SPIN_CAP) { atomicAdd(&(bar)[XB_TMO], 1u); break; } } } } while (0)
; __device__ __forceinline__ void xcd_barrier(const XcdBarrier& b) {
;     ...
;         unsigned nloc = b.st[0], nx = b.st[1];
;         if (nloc == 0u) { xcd_barrier_complete(bar, b.x, nloc, nx); b.st[0] = nloc; b.st[1] = nx; }
;         const unsigned old = xb_add(&bar[XB_XSUB(b.x)], 1u);
;         const unsigned gen = old / nloc;
;         if (old + 1u == (gen + 1u) * nloc) {
;             __builtin_amdgcn_fence(__ATOMIC_RELEASE, "agent");
;             asm volatile("s_waitcnt vmcnt(0)" ::: "memory");
;             const unsigned og = xb_add(&bar[XB_TOP], 1u);
;             const unsigned tg = og / nx;
;             if (og + 1u == (tg + 1u) * nx) xb_add(&bar[XB_TOPGEN], 1u);
;             else XB_SPIN(xb_ld(&bar[XB_TOPGEN]) == tg, bar);
;             __builtin_amdgcn_fence(__ATOMIC_ACQUIRE, "agent");
;             xb_add(&bar[XB_XGEN(b.x)], 1u);
;             asm volatile("s_waitcnt vmcnt(0)" ::: "memory");
;         } else {
;             XB_SPIN(xb_ld(&bar[XB_XGEN(b.x)]) == gen, bar);
;             __builtin_amdgcn_fence(__ATOMIC_ACQUIRE, "agent");
;             asm volatile("s_waitcnt vmcnt(0)" ::: "memory");
.LBB0_65:
	v_readlane_b32 s2, v253, 6
	s_lshl_b32 s2, s2, 8
	v_readlane_b32 s4, v253, 4
	v_readlane_b32 s5, v253, 5
	s_add_u32 s2, s4, s2
	s_addc_u32 s3, s5, 0
	v_mov_b32_e32 v2, 0x1000
	v_mov_b32_e32 v4, 1
	global_atomic_add v4, v2, v4, s[2:3] offset:1024 sc0
	v_cvt_f32_u32_e32 v2, v3
	v_sub_u32_e32 v5, 0, v3
	v_rcp_iflag_f32_e32 v2, v2
	s_nop 0
	v_mul_f32_e32 v2, 0x4f7ffffe, v2
	v_cvt_u32_f32_e32 v2, v2
	v_mul_lo_u32 v5, v5, v2
	v_mul_hi_u32 v5, v2, v5
	v_add_u32_e32 v2, v2, v5
	s_waitcnt vmcnt(0)
	v_mul_hi_u32 v2, v4, v2
	v_mul_lo_u32 v5, v2, v3
	v_sub_u32_e32 v5, v4, v5
	v_add_u32_e32 v6, 1, v2
	v_cmp_ge_u32_e32 vcc, v5, v3
	v_add_u32_e32 v4, 1, v4
	s_nop 0
	v_cndmask_b32_e32 v2, v2, v6, vcc
	v_sub_u32_e32 v6, v5, v3
	v_cndmask_b32_e32 v5, v5, v6, vcc
	v_add_u32_e32 v6, 1, v2
	v_cmp_ge_u32_e32 vcc, v5, v3
	s_nop 1
	v_cndmask_b32_e32 v2, v2, v6, vcc
	v_mul_lo_u32 v5, v3, v2
	v_add_u32_e32 v3, v5, v3
	v_cmp_ne_u32_e32 vcc, v4, v3
	s_and_saveexec_b64 s[4:5], vcc
	s_xor_b64 s[4:5], exec, s[4:5]
	s_cbranch_execz .LBB0_79
	s_waitcnt lgkmcnt(0)
	v_mov_b32_e32 v1, 0x2000
	buffer_inv sc1
	global_load_dword v1, v1, s[2:3] offset:1024 sc1
	s_add_u32 s10, s2, 0x2400
	s_addc_u32 s11, s3, 0
	s_waitcnt vmcnt(0)
	v_cmp_eq_u32_e32 vcc, v1, v2
	s_and_saveexec_b64 s[6:7], vcc
	s_cbranch_execz .LBB0_78
	s_add_u32 s8, s94, 0x4200
	s_addc_u32 s9, s95, 0
	s_mov_b32 s22, 1
	s_mov_b64 s[12:13], 0
	v_mov_b32_e32 v1, 0
	s_branch .LBB0_69

; __device__ __forceinline__ unsigned xb_ld(unsigned* p)              { return __hip_atomic_load(p, __ATOMIC_RELAXED, __HIP_MEMORY_SCOPE_AGENT); }
; __device__ __forceinline__ unsigned xb_add(unsigned* p, unsigned v) { return __hip_atomic_fetch_add(p, v, __ATOMIC_RELAXED, __HIP_MEMORY_SCOPE_AGENT); }
; #define XB_SPIN(cond, bar) do { unsigned _sp = 0; while (cond) { __builtin_amdgcn_s_sleep(1); \
;     if ((++_sp & 255u) == 0u) { if (xb_ld(&(bar)[XB_TMO])) break; if (_sp > XB_SPIN_CAP) { atomicAdd(&(bar)[XB_TMO], 1u); break; } } } } while (0)
; __device__ __forceinline__ void xcd_barrier(const XcdBarrier& b) {
;     ...
;         unsigned nloc = b.st[0], nx = b.st[1];
;         if (nloc == 0u) { xcd_barrier_complete(bar, b.x, nloc, nx); b.st[0] = nloc; b.st[1] = nx; }
;         const unsigned old = xb_add(&bar[XB_XSUB(b.x)], 1u);
;         const unsigned gen = old / nloc;
;         if (old + 1u == (gen + 1u) * nloc) {
;             __builtin_amdgcn_fence(__ATOMIC_RELEASE, "agent");
;             asm volatile("s_waitcnt vmcnt(0)" ::: "memory");
;             const unsigned og = xb_add(&bar[XB_TOP], 1u);
;             const unsigned tg = og / nx;
;             if (og + 1u == (tg + 1u) * nx) xb_add(&bar[XB_TOPGEN], 1u);
;             else XB_SPIN(xb_ld(&bar[XB_TOPGEN]) == tg, bar);
;             __builtin_amdgcn_fence(__ATOMIC_ACQUIRE, "agent");
;             xb_add(&bar[XB_XGEN(b.x)], 1u);
;             asm volatile("s_waitcnt vmcnt(0)" ::: "memory");
;         } else {
;             XB_SPIN(xb_ld(&bar[XB_XGEN(b.x)]) == gen, bar);
;             __builtin_amdgcn_fence(__ATOMIC_ACQUIRE, "agent");
;             asm volatile("s_waitcnt vmcnt(0)" ::: "memory");
.LBB0_226:
	v_readlane_b32 s2, v253, 6
	s_lshl_b32 s2, s2, 8
	v_readlane_b32 s4, v253, 4
	v_readlane_b32 s5, v253, 5
	s_add_u32 s2, s4, s2
	s_addc_u32 s3, s5, 0
	v_mov_b32_e32 v3, 0x1000
	v_mov_b32_e32 v5, 1
	global_atomic_add v5, v3, v5, s[2:3] offset:1024 sc0
	v_cvt_f32_u32_e32 v3, v4
	v_sub_u32_e32 v6, 0, v4
	v_rcp_iflag_f32_e32 v3, v3
	s_nop 0
	v_mul_f32_e32 v3, 0x4f7ffffe, v3
	v_cvt_u32_f32_e32 v3, v3
	v_mul_lo_u32 v6, v6, v3
	v_mul_hi_u32 v6, v3, v6
	v_add_u32_e32 v3, v3, v6
	s_waitcnt vmcnt(0)
	v_mul_hi_u32 v3, v5, v3
	v_mul_lo_u32 v6, v3, v4
	v_sub_u32_e32 v6, v5, v6
	v_add_u32_e32 v7, 1, v3
	v_cmp_ge_u32_e32 vcc, v6, v4
	v_add_u32_e32 v5, 1, v5
	s_nop 0
	v_cndmask_b32_e32 v3, v3, v7, vcc
	v_sub_u32_e32 v7, v6, v4
	v_cndmask_b32_e32 v6, v6, v7, vcc
	v_add_u32_e32 v7, 1, v3
	v_cmp_ge_u32_e32 vcc, v6, v4
	s_nop 1
	v_cndmask_b32_e32 v3, v3, v7, vcc
	v_mul_lo_u32 v6, v4, v3
	v_add_u32_e32 v4, v6, v4
	v_cmp_ne_u32_e32 vcc, v5, v4
	s_and_saveexec_b64 s[4:5], vcc
	s_xor_b64 s[4:5], exec, s[4:5]
	s_cbranch_execz .LBB0_240
	s_waitcnt lgkmcnt(0)
	v_mov_b32_e32 v2, 0x2000
	buffer_inv sc1
	global_load_dword v2, v2, s[2:3] offset:1024 sc1
	s_add_u32 s10, s2, 0x2400
	s_addc_u32 s11, s3, 0
	s_waitcnt vmcnt(0)
	v_cmp_eq_u32_e32 vcc, v2, v3
	s_and_saveexec_b64 s[6:7], vcc
	s_cbranch_execz .LBB0_239
	s_add_u32 s8, s94, 0x4200
	s_addc_u32 s9, s95, 0
	s_mov_b32 s22, 1
	s_mov_b64 s[12:13], 0
	v_mov_b32_e32 v2, 0
	s_branch .LBB0_230

; __device__ __forceinline__ unsigned xb_add(unsigned* p, unsigned v) { return __hip_atomic_fetch_add(p, v, __ATOMIC_RELAXED, __HIP_MEMORY_SCOPE_AGENT); }
; __device__ __forceinline__ void xcd_barrier(const XcdBarrier& b) {
;     ...
;             __builtin_amdgcn_fence(__ATOMIC_ACQUIRE, "agent");
;             xb_add(&bar[XB_XGEN(b.x)], 1u);
;             asm volatile("s_waitcnt vmcnt(0)" ::: "memory");
.LBB0_2202:
	s_or_b64 exec, exec, s[42:43]
	v_readlane_b32 s12, v254, 13
	v_readlane_b32 s13, v254, 14
	s_waitcnt vmcnt(0)
	s_nop 0
	s_nop 2
	global_atomic_add v133, v171, s[12:13]
	s_waitcnt vmcnt(0)

; __device__ __forceinline__ unsigned xb_ld(unsigned* p)              { return __hip_atomic_load(p, __ATOMIC_RELAXED, __HIP_MEMORY_SCOPE_AGENT); }
; __device__ __forceinline__ unsigned xb_add(unsigned* p, unsigned v) { return __hip_atomic_fetch_add(p, v, __ATOMIC_RELAXED, __HIP_MEMORY_SCOPE_AGENT); }
; #define XB_SPIN(cond, bar) do { unsigned _sp = 0; while (cond) { __builtin_amdgcn_s_sleep(1); \
;     if ((++_sp & 255u) == 0u) { if (xb_ld(&(bar)[XB_TMO])) break; if (_sp > XB_SPIN_CAP) { atomicAdd(&(bar)[XB_TMO], 1u); break; } } } } while (0)
; __device__ __forceinline__ void xcd_barrier(const XcdBarrier& b) {
;     ...
;         unsigned nloc = b.st[0], nx = b.st[1];
;         if (nloc == 0u) { xcd_barrier_complete(bar, b.x, nloc, nx); b.st[0] = nloc; b.st[1] = nx; }
;         const unsigned old = xb_add(&bar[XB_XSUB(b.x)], 1u);
;         const unsigned gen = old / nloc;
;         if (old + 1u == (gen + 1u) * nloc) {
;             __builtin_amdgcn_fence(__ATOMIC_RELEASE, "agent");
;             asm volatile("s_waitcnt vmcnt(0)" ::: "memory");
;             const unsigned og = xb_add(&bar[XB_TOP], 1u);
;             const unsigned tg = og / nx;
;             if (og + 1u == (tg + 1u) * nx) xb_add(&bar[XB_TOPGEN], 1u);
;             else XB_SPIN(xb_ld(&bar[XB_TOPGEN]) == tg, bar);
;             __builtin_amdgcn_fence(__ATOMIC_ACQUIRE, "agent");
;             xb_add(&bar[XB_XGEN(b.x)], 1u);
;             asm volatile("s_waitcnt vmcnt(0)" ::: "memory");
;         } else {
;             XB_SPIN(xb_ld(&bar[XB_XGEN(b.x)]) == gen, bar);
.LBB0_2295:
	v_readlane_b32 s12, v255, 7
	v_readlane_b32 s13, v255, 8
	v_cvt_f32_u32_e32 v3, v4
	v_sub_u32_e32 v6, 0, v4
	v_rcp_iflag_f32_e32 v3, v3
	s_nop 1
	global_atomic_add v5, v133, v171, s[12:13] sc0
	v_mul_f32_e32 v3, 0x4f7ffffe, v3
	v_cvt_u32_f32_e32 v3, v3
	v_mul_lo_u32 v6, v6, v3
	v_mul_hi_u32 v6, v3, v6
	v_add_u32_e32 v3, v3, v6
	s_waitcnt vmcnt(0)
	v_mul_hi_u32 v3, v5, v3
	v_mul_lo_u32 v6, v3, v4
	v_sub_u32_e32 v6, v5, v6
	v_add_u32_e32 v7, 1, v3
	v_cmp_ge_u32_e32 vcc, v6, v4
	v_add_u32_e32 v5, 1, v5
	s_nop 0
	v_cndmask_b32_e32 v3, v3, v7, vcc
	v_sub_u32_e32 v7, v6, v4
	v_cndmask_b32_e32 v6, v6, v7, vcc
	v_add_u32_e32 v7, 1, v3
	v_cmp_ge_u32_e32 vcc, v6, v4
	s_nop 1
	v_cndmask_b32_e32 v3, v3, v7, vcc
	v_mul_lo_u32 v6, v4, v3
	v_add_u32_e32 v4, v6, v4
	v_cmp_ne_u32_e32 vcc, v5, v4
	s_and_saveexec_b64 s[12:13], vcc
	s_xor_b64 s[42:43], exec, s[12:13]
	s_cbranch_execz .LBB0_2309
	v_readlane_b32 s12, v254, 13
	v_readlane_b32 s13, v254, 14
	s_waitcnt lgkmcnt(0)
	s_nop 3
	buffer_inv sc1
	global_load_dword v2, v133, s[12:13] sc1
	s_waitcnt vmcnt(0)
	v_cmp_eq_u32_e32 vcc, v2, v3
	s_and_saveexec_b64 s[46:47], vcc
	s_cbranch_execz .LBB0_2308
	s_mov_b32 s2, 1
	s_mov_b64 s[66:67], 0
	s_branch .LBB0_2299

; __device__ __forceinline__ unsigned xb_ld(unsigned* p)              { return __hip_atomic_load(p, __ATOMIC_RELAXED, __HIP_MEMORY_SCOPE_AGENT); }
; __device__ __forceinline__ unsigned xb_add(unsigned* p, unsigned v) { return __hip_atomic_fetch_add(p, v, __ATOMIC_RELAXED, __HIP_MEMORY_SCOPE_AGENT); }
; #define XB_SPIN(cond, bar) do { unsigned _sp = 0; while (cond) { __builtin_amdgcn_s_sleep(1); \
;     if ((++_sp & 255u) == 0u) { if (xb_ld(&(bar)[XB_TMO])) break; if (_sp > XB_SPIN_CAP) { atomicAdd(&(bar)[XB_TMO], 1u); break; } } } } while (0)
; __device__ __forceinline__ void xcd_barrier(const XcdBarrier& b) {
;     ...
;             __builtin_amdgcn_fence(__ATOMIC_RELEASE, "agent");
;             asm volatile("s_waitcnt vmcnt(0)" ::: "memory");
;             const unsigned og = xb_add(&bar[XB_TOP], 1u);
;             const unsigned tg = og / nx;
;             if (og + 1u == (tg + 1u) * nx) xb_add(&bar[XB_TOPGEN], 1u);
;             else XB_SPIN(xb_ld(&bar[XB_TOPGEN]) == tg, bar);
;             __builtin_amdgcn_fence(__ATOMIC_ACQUIRE, "agent");
;             xb_add(&bar[XB_XGEN(b.x)], 1u);
;             asm volatile("s_waitcnt vmcnt(0)" ::: "memory");
;         } else {
;             XB_SPIN(xb_ld(&bar[XB_XGEN(b.x)]) == gen, bar);
;             __builtin_amdgcn_fence(__ATOMIC_ACQUIRE, "agent");
;             asm volatile("s_waitcnt vmcnt(0)" ::: "memory");
;         }
.LBB0_2308:
	s_or_b64 exec, exec, s[46:47]
	s_waitcnt vmcnt(0)
	s_waitcnt vmcnt(0)
.LBB0_2309:
	s_andn2_saveexec_b64 s[12:13], s[42:43]
	s_cbranch_execz .LBB0_2203
	s_mov_b64 s[42:43], exec
	buffer_wbl2 sc1
	buffer_inv sc1
	s_waitcnt lgkmcnt(0)
	s_waitcnt vmcnt(0)
	v_mbcnt_lo_u32_b32 v3, s42, 0
	v_mbcnt_hi_u32_b32 v3, s43, v3
	v_cmp_eq_u32_e32 vcc, 0, v3
	s_and_saveexec_b64 s[46:47], vcc
	s_cbranch_execz .LBB0_2312
	s_bcnt1_i32_b64 s2, s[42:43]
	v_readlane_b32 s12, v255, 9
	v_mov_b32_e32 v4, s2
	v_readlane_b32 s13, v255, 10
	s_nop 4
	global_atomic_add v4, v133, v4, s[12:13] sc0

; __device__ __forceinline__ unsigned xb_ld(unsigned* p)              { return __hip_atomic_load(p, __ATOMIC_RELAXED, __HIP_MEMORY_SCOPE_AGENT); }
; __device__ __forceinline__ unsigned xb_add(unsigned* p, unsigned v) { return __hip_atomic_fetch_add(p, v, __ATOMIC_RELAXED, __HIP_MEMORY_SCOPE_AGENT); }
; #define XB_SPIN(cond, bar) do { unsigned _sp = 0; while (cond) { __builtin_amdgcn_s_sleep(1); \
;     if ((++_sp & 255u) == 0u) { if (xb_ld(&(bar)[XB_TMO])) break; if (_sp > XB_SPIN_CAP) { atomicAdd(&(bar)[XB_TMO], 1u); break; } } } } while (0)
; __device__ __forceinline__ void xcd_barrier(const XcdBarrier& b) {
;     ...
;         unsigned nloc = b.st[0], nx = b.st[1];
;         if (nloc == 0u) { xcd_barrier_complete(bar, b.x, nloc, nx); b.st[0] = nloc; b.st[1] = nx; }
;         const unsigned old = xb_add(&bar[XB_XSUB(b.x)], 1u);
;         const unsigned gen = old / nloc;
;         if (old + 1u == (gen + 1u) * nloc) {
;             __builtin_amdgcn_fence(__ATOMIC_RELEASE, "agent");
;             asm volatile("s_waitcnt vmcnt(0)" ::: "memory");
;             const unsigned og = xb_add(&bar[XB_TOP], 1u);
;             const unsigned tg = og / nx;
;             if (og + 1u == (tg + 1u) * nx) xb_add(&bar[XB_TOPGEN], 1u);
;             else XB_SPIN(xb_ld(&bar[XB_TOPGEN]) == tg, bar);
;             __builtin_amdgcn_fence(__ATOMIC_ACQUIRE, "agent");
;             xb_add(&bar[XB_XGEN(b.x)], 1u);
;             asm volatile("s_waitcnt vmcnt(0)" ::: "memory");
;         } else {
;             XB_SPIN(xb_ld(&bar[XB_XGEN(b.x)]) == gen, bar);
;             __builtin_amdgcn_fence(__ATOMIC_ACQUIRE, "agent");
;             asm volatile("s_waitcnt vmcnt(0)" ::: "memory");
.LBB0_4431:
	v_readlane_b32 s0, v253, 6
	s_lshl_b32 s0, s0, 8
	v_readlane_b32 s4, v253, 4
	v_readlane_b32 s5, v253, 5
	s_add_u32 s0, s4, s0
	s_addc_u32 s1, s5, 0
	v_mov_b32_e32 v2, 0x1000
	v_mov_b32_e32 v4, 1
	global_atomic_add v4, v2, v4, s[0:1] offset:1024 sc0
	v_cvt_f32_u32_e32 v2, v3
	v_sub_u32_e32 v5, 0, v3
	v_rcp_iflag_f32_e32 v2, v2
	s_nop 0
	v_mul_f32_e32 v2, 0x4f7ffffe, v2
	v_cvt_u32_f32_e32 v2, v2
	v_mul_lo_u32 v5, v5, v2
	v_mul_hi_u32 v5, v2, v5
	v_add_u32_e32 v2, v2, v5
	s_waitcnt vmcnt(0)
	v_mul_hi_u32 v2, v4, v2
	v_mul_lo_u32 v5, v2, v3
	v_sub_u32_e32 v5, v4, v5
	v_add_u32_e32 v6, 1, v2
	v_cmp_ge_u32_e32 vcc, v5, v3
	v_add_u32_e32 v4, 1, v4
	s_nop 0
	v_cndmask_b32_e32 v2, v2, v6, vcc
	v_sub_u32_e32 v6, v5, v3
	v_cndmask_b32_e32 v5, v5, v6, vcc
	v_add_u32_e32 v6, 1, v2
	v_cmp_ge_u32_e32 vcc, v5, v3
	s_nop 1
	v_cndmask_b32_e32 v2, v2, v6, vcc
	v_mul_lo_u32 v5, v3, v2
	v_add_u32_e32 v3, v5, v3
	v_cmp_ne_u32_e32 vcc, v4, v3
	s_and_saveexec_b64 s[4:5], vcc
	s_xor_b64 s[4:5], exec, s[4:5]
	s_cbranch_execz .LBB0_4445
	s_waitcnt lgkmcnt(0)
	v_mov_b32_e32 v1, 0x2000
	buffer_inv sc1
	global_load_dword v1, v1, s[0:1] offset:1024 sc1
	s_add_u32 s10, s0, 0x2400
	s_addc_u32 s11, s1, 0
	s_waitcnt vmcnt(0)
	v_cmp_eq_u32_e32 vcc, v1, v2
	s_and_saveexec_b64 s[6:7], vcc
	s_cbranch_execz .LBB0_4444
	s_add_u32 s8, s94, 0x4200
	s_addc_u32 s9, s95, 0
	s_mov_b32 s22, 1
	s_mov_b64 s[12:13], 0
	v_mov_b32_e32 v1, 0
	s_branch .LBB0_4435

; __device__ __forceinline__ unsigned xb_add(unsigned* p, unsigned v) { return __hip_atomic_fetch_add(p, v, __ATOMIC_RELAXED, __HIP_MEMORY_SCOPE_AGENT); }
; __device__ __forceinline__ void xcd_barrier(const XcdBarrier& b) {
;     ...
;             __builtin_amdgcn_fence(__ATOMIC_ACQUIRE, "agent");
;             xb_add(&bar[XB_XGEN(b.x)], 1u);
;             asm volatile("s_waitcnt vmcnt(0)" ::: "memory");
.LBB0_4465:
	s_or_b64 exec, exec, s[22:23]
	v_readlane_b32 s0, v253, 8
	v_readlane_b32 s1, v253, 9
	s_waitcnt vmcnt(0)
	s_nop 0
	s_nop 2
	global_atomic_add v133, v171, s[0:1]
	s_waitcnt vmcnt(0)

; __device__ __forceinline__ unsigned xb_ld(unsigned* p)              { return __hip_atomic_load(p, __ATOMIC_RELAXED, __HIP_MEMORY_SCOPE_AGENT); }
; __device__ __forceinline__ unsigned xb_add(unsigned* p, unsigned v) { return __hip_atomic_fetch_add(p, v, __ATOMIC_RELAXED, __HIP_MEMORY_SCOPE_AGENT); }
; #define XB_SPIN(cond, bar) do { unsigned _sp = 0; while (cond) { __builtin_amdgcn_s_sleep(1); \
;     if ((++_sp & 255u) == 0u) { if (xb_ld(&(bar)[XB_TMO])) break; if (_sp > XB_SPIN_CAP) { atomicAdd(&(bar)[XB_TMO], 1u); break; } } } } while (0)
; __device__ __forceinline__ void xcd_barrier(const XcdBarrier& b) {
;     ...
;         unsigned nloc = b.st[0], nx = b.st[1];
;         if (nloc == 0u) { xcd_barrier_complete(bar, b.x, nloc, nx); b.st[0] = nloc; b.st[1] = nx; }
;         const unsigned old = xb_add(&bar[XB_XSUB(b.x)], 1u);
;         const unsigned gen = old / nloc;
;         if (old + 1u == (gen + 1u) * nloc) {
;             __builtin_amdgcn_fence(__ATOMIC_RELEASE, "agent");
;             asm volatile("s_waitcnt vmcnt(0)" ::: "memory");
;             const unsigned og = xb_add(&bar[XB_TOP], 1u);
;             const unsigned tg = og / nx;
;             if (og + 1u == (tg + 1u) * nx) xb_add(&bar[XB_TOPGEN], 1u);
;             else XB_SPIN(xb_ld(&bar[XB_TOPGEN]) == tg, bar);
;             __builtin_amdgcn_fence(__ATOMIC_ACQUIRE, "agent");
;             xb_add(&bar[XB_XGEN(b.x)], 1u);
;             asm volatile("s_waitcnt vmcnt(0)" ::: "memory");
;         } else {
;             XB_SPIN(xb_ld(&bar[XB_XGEN(b.x)]) == gen, bar);
.LBB0_4558:
	v_readlane_b32 s0, v255, 37
	v_readlane_b32 s1, v255, 38
	v_cvt_f32_u32_e32 v3, v4
	v_sub_u32_e32 v6, 0, v4
	v_rcp_iflag_f32_e32 v3, v3
	s_nop 1
	global_atomic_add v5, v133, v171, s[0:1] sc0
	v_mul_f32_e32 v3, 0x4f7ffffe, v3
	v_cvt_u32_f32_e32 v3, v3
	v_mul_lo_u32 v6, v6, v3
	v_mul_hi_u32 v6, v3, v6
	v_add_u32_e32 v3, v3, v6
	s_waitcnt vmcnt(0)
	v_mul_hi_u32 v3, v5, v3
	v_mul_lo_u32 v6, v3, v4
	v_sub_u32_e32 v6, v5, v6
	v_add_u32_e32 v7, 1, v3
	v_cmp_ge_u32_e32 vcc, v6, v4
	v_add_u32_e32 v5, 1, v5
	s_nop 0
	v_cndmask_b32_e32 v3, v3, v7, vcc
	v_sub_u32_e32 v7, v6, v4
	v_cndmask_b32_e32 v6, v6, v7, vcc
	v_add_u32_e32 v7, 1, v3
	v_cmp_ge_u32_e32 vcc, v6, v4
	s_nop 1
	v_cndmask_b32_e32 v3, v3, v7, vcc
	v_mul_lo_u32 v6, v4, v3
	v_add_u32_e32 v4, v6, v4
	v_cmp_ne_u32_e32 vcc, v5, v4
	s_and_saveexec_b64 s[0:1], vcc
	s_xor_b64 s[22:23], exec, s[0:1]
	s_cbranch_execz .LBB0_4572
	v_readlane_b32 s0, v253, 8
	v_readlane_b32 s1, v253, 9
	s_waitcnt lgkmcnt(0)
	s_nop 3
	buffer_inv sc1
	global_load_dword v2, v133, s[0:1] sc1
	s_waitcnt vmcnt(0)
	v_cmp_eq_u32_e32 vcc, v2, v3
	s_and_saveexec_b64 s[38:39], vcc
	s_cbranch_execz .LBB0_4571
	s_mov_b32 s0, 1
	s_mov_b64 s[40:41], 0
	s_branch .LBB0_4562

; __device__ __forceinline__ unsigned xb_ld(unsigned* p)              { return __hip_atomic_load(p, __ATOMIC_RELAXED, __HIP_MEMORY_SCOPE_AGENT); }
; __device__ __forceinline__ unsigned xb_add(unsigned* p, unsigned v) { return __hip_atomic_fetch_add(p, v, __ATOMIC_RELAXED, __HIP_MEMORY_SCOPE_AGENT); }
; #define XB_SPIN(cond, bar) do { unsigned _sp = 0; while (cond) { __builtin_amdgcn_s_sleep(1); \
;     if ((++_sp & 255u) == 0u) { if (xb_ld(&(bar)[XB_TMO])) break; if (_sp > XB_SPIN_CAP) { atomicAdd(&(bar)[XB_TMO], 1u); break; } } } } while (0)
; __device__ __forceinline__ void xcd_barrier(const XcdBarrier& b) {
;     ...
;             __builtin_amdgcn_fence(__ATOMIC_RELEASE, "agent");
;             asm volatile("s_waitcnt vmcnt(0)" ::: "memory");
;             const unsigned og = xb_add(&bar[XB_TOP], 1u);
;             const unsigned tg = og / nx;
;             if (og + 1u == (tg + 1u) * nx) xb_add(&bar[XB_TOPGEN], 1u);
;             else XB_SPIN(xb_ld(&bar[XB_TOPGEN]) == tg, bar);
;             __builtin_amdgcn_fence(__ATOMIC_ACQUIRE, "agent");
;             xb_add(&bar[XB_XGEN(b.x)], 1u);
;             asm volatile("s_waitcnt vmcnt(0)" ::: "memory");
;         } else {
;             XB_SPIN(xb_ld(&bar[XB_XGEN(b.x)]) == gen, bar);
;             __builtin_amdgcn_fence(__ATOMIC_ACQUIRE, "agent");
;             asm volatile("s_waitcnt vmcnt(0)" ::: "memory");
;         }
.LBB0_4571:
	s_or_b64 exec, exec, s[38:39]
	s_waitcnt vmcnt(0)
	s_waitcnt vmcnt(0)
.LBB0_4572:
	s_andn2_saveexec_b64 s[0:1], s[22:23]
	s_cbranch_execz .LBB0_4466
	s_mov_b64 s[22:23], exec
	buffer_wbl2 sc1
	buffer_inv sc1
	s_waitcnt lgkmcnt(0)
	s_waitcnt vmcnt(0)
	v_mbcnt_lo_u32_b32 v3, s22, 0
	v_mbcnt_hi_u32_b32 v3, s23, v3
	v_cmp_eq_u32_e32 vcc, 0, v3
	s_and_saveexec_b64 s[38:39], vcc
	s_cbranch_execz .LBB0_4575
	s_bcnt1_i32_b64 s0, s[22:23]
	v_mov_b32_e32 v4, s0
	v_readlane_b32 s0, v254, 57
	v_readlane_b32 s1, v254, 58
	s_nop 4
	global_atomic_add v4, v133, v4, s[0:1] sc0
